# GEMM load segments: M0 write before the address add (no s_nop) and merged vmcnt+lgkmcnt wait (without the saddr conversion)
# baseline (speedup 1.0000x reference)
.LBB0_514:
	s_add_u32 s22, s82, s92
	s_addc_u32 s23, s83, s93
	s_add_u32 s24, s22, 0x100
	s_addc_u32 s25, s23, 0
	s_add_u32 s58, s3, s92
	s_addc_u32 s59, s2, s93
	s_add_i32 vcc_lo, 0, 0x10000
	s_cmpk_eq_i32 s92, 0xf00
	s_cselect_b64 s[26:27], -1, 0
	s_and_b64 s[22:23], s[26:27], exec
	s_cselect_b32 s25, s67, s25
	s_cselect_b32 s24, s75, s24
	s_cselect_b32 s23, s95, s59
	s_cselect_b32 s22, s29, s58
	s_add_i32 vcc_hi, 0, 0x14000
	v_add_u32_e32 v130, vcc_lo, v223
	v_add_u32_e32 v142, vcc_hi, v223
	ds_read_b128 v[146:149], v130
	ds_read_b128 v[150:153], v130 offset:1024
	ds_read_b128 v[154:157], v130 offset:2048
	ds_read_b128 v[158:161], v130 offset:3072
	ds_read_b128 v[130:133], v142
	ds_read_b128 v[134:137], v142 offset:1024
	ds_read_b128 v[138:141], v142 offset:2048
	ds_read_b128 v[142:145], v142 offset:3072
	v_lshl_add_u64 v[214:215], v[210:211], 0, s[92:93]
	s_add_i32 m0, s81, 0xc000
	ds_read_b128 v[162:165], v224
	ds_read_b128 v[166:169], v224 offset:1024
	ds_read_b128 v[170:173], v224 offset:2048
	ds_read_b128 v[174:177], v224 offset:3072
	ds_read_b128 v[178:181], v224 offset:4096
	ds_read_b128 v[182:185], v224 offset:5120
	ds_read_b128 v[186:189], v224 offset:6144
	ds_read_b128 v[190:193], v224 offset:7168
	global_load_lds_dwordx4 v[214:215], off
	s_add_i32 m0, s81, 0xe000
	v_lshl_add_u64 v[214:215], v[212:213], 0, s[92:93]
	global_load_lds_dwordx4 v[214:215], off
	s_waitcnt vmcnt(8) lgkmcnt(0)
	s_barrier
	v_mfma_f32_16x16x32_bf16 v[124:127], v[146:149], v[162:165], v[124:127]
	v_mfma_f32_16x16x32_bf16 v[120:123], v[154:157], v[162:165], v[120:123]
	v_mfma_f32_16x16x32_bf16 v[116:119], v[146:149], v[170:173], v[116:119]
	v_mfma_f32_16x16x32_bf16 v[108:111], v[154:157], v[170:173], v[108:111]
	v_mfma_f32_16x16x32_bf16 v[100:103], v[146:149], v[178:181], v[100:103]
	v_mfma_f32_16x16x32_bf16 v[92:95], v[154:157], v[178:181], v[92:95]
	v_mfma_f32_16x16x32_bf16 v[84:87], v[146:149], v[186:189], v[84:87]
	v_mfma_f32_16x16x32_bf16 v[76:79], v[154:157], v[186:189], v[76:79]
	v_mfma_f32_16x16x32_bf16 v[124:127], v[150:153], v[166:169], v[124:127]
	v_mfma_f32_16x16x32_bf16 v[120:123], v[158:161], v[166:169], v[120:123]
	v_mfma_f32_16x16x32_bf16 v[116:119], v[150:153], v[174:177], v[116:119]
	v_mfma_f32_16x16x32_bf16 v[108:111], v[158:161], v[174:177], v[108:111]
	v_mfma_f32_16x16x32_bf16 v[100:103], v[150:153], v[182:185], v[100:103]
	v_mfma_f32_16x16x32_bf16 v[92:95], v[158:161], v[182:185], v[92:95]
	v_mfma_f32_16x16x32_bf16 v[84:87], v[150:153], v[190:193], v[84:87]
	v_mfma_f32_16x16x32_bf16 v[76:79], v[158:161], v[190:193], v[76:79]
	v_mfma_f32_16x16x32_bf16 v[112:115], v[130:133], v[162:165], v[112:115]
	v_mfma_f32_16x16x32_bf16 v[104:107], v[138:141], v[162:165], v[104:107]
	v_mfma_f32_16x16x32_bf16 v[96:99], v[130:133], v[170:173], v[96:99]
	v_mfma_f32_16x16x32_bf16 v[88:91], v[138:141], v[170:173], v[88:91]
	v_mfma_f32_16x16x32_bf16 v[80:83], v[130:133], v[178:181], v[80:83]
	v_mfma_f32_16x16x32_bf16 v[72:75], v[138:141], v[178:181], v[72:75]
	v_mfma_f32_16x16x32_bf16 v[68:71], v[130:133], v[186:189], v[68:71]
	v_mfma_f32_16x16x32_bf16 v[64:67], v[138:141], v[186:189], v[64:67]
	v_mfma_f32_16x16x32_bf16 v[112:115], v[134:137], v[166:169], v[112:115]
	v_mfma_f32_16x16x32_bf16 v[104:107], v[142:145], v[166:169], v[104:107]
	v_mfma_f32_16x16x32_bf16 v[96:99], v[134:137], v[174:177], v[96:99]
	v_mfma_f32_16x16x32_bf16 v[88:91], v[142:145], v[174:177], v[88:91]
	v_mfma_f32_16x16x32_bf16 v[80:83], v[134:137], v[182:185], v[80:83]
	v_mfma_f32_16x16x32_bf16 v[72:75], v[142:145], v[182:185], v[72:75]
	v_mfma_f32_16x16x32_bf16 v[68:71], v[134:137], v[190:193], v[68:71]
	v_mfma_f32_16x16x32_bf16 v[64:67], v[142:145], v[190:193], v[64:67]
	s_barrier
	s_add_i32 s58, vcc_lo, s28
	v_lshl_add_u64 v[214:215], s[22:23], 0, v[200:201]
	s_mov_b32 m0, s58
	ds_read_b128 v[186:189], v224 offset:16384
	ds_read_b128 v[190:193], v224 offset:17408
	ds_read_b128 v[178:181], v224 offset:18432
	ds_read_b128 v[182:185], v224 offset:19456
	ds_read_b128 v[170:173], v224 offset:20480
	ds_read_b128 v[174:177], v224 offset:21504
	ds_read_b128 v[162:165], v224 offset:22528
	ds_read_b128 v[166:169], v224 offset:23552
	global_load_lds_dwordx4 v[214:215], off
	s_add_i32 m0, s58, 0x2000
	s_add_u32 s58, s22, 0x80000
	v_lshl_add_u64 v[216:217], s[22:23], 0, v[204:205]
	s_addc_u32 s59, s23, 0
	s_add_i32 vcc_lo, vcc_hi, s28
	global_load_lds_dwordx4 v[216:217], off
	v_lshl_add_u64 v[218:219], s[58:59], 0, v[200:201]
	s_mov_b32 m0, vcc_lo
	v_lshl_add_u64 v[220:221], s[24:25], 0, v[202:203]
	global_load_lds_dwordx4 v[218:219], off
	v_lshl_add_u64 v[218:219], s[58:59], 0, v[204:205]
	s_add_i32 m0, vcc_lo, 0x2000
	v_cndmask_b32_e64 v194, 0, 1, s[96:97]
	global_load_lds_dwordx4 v[218:219], off
	v_lshl_add_u64 v[218:219], s[24:25], 0, v[198:199]
	s_mov_b32 m0, s81
	v_cmp_ne_u32_e64 s[58:59], 1, v194
	global_load_lds_dwordx4 v[218:219], off
	s_mov_b32 m0, s88
	s_andn2_b64 vcc, exec, s[96:97]
	global_load_lds_dwordx4 v[220:221], off
	s_waitcnt vmcnt(8) lgkmcnt(0)
	s_barrier
	s_cbranch_vccnz .LBB0_516
	s_waitcnt lgkmcnt(0)
	v_mfma_f32_16x16x32_bf16 v[60:63], v[146:149], v[186:189], v[60:63]
	v_mfma_f32_16x16x32_bf16 v[56:59], v[154:157], v[186:189], v[56:59]
	v_mfma_f32_16x16x32_bf16 v[44:47], v[146:149], v[178:181], v[44:47]
	v_mfma_f32_16x16x32_bf16 v[40:43], v[154:157], v[178:181], v[40:43]
	v_mfma_f32_16x16x32_bf16 v[28:31], v[146:149], v[170:173], v[28:31]
	v_mfma_f32_16x16x32_bf16 v[24:27], v[154:157], v[170:173], v[24:27]
	v_mfma_f32_16x16x32_bf16 v[12:15], v[146:149], v[162:165], v[12:15]
	v_mfma_f32_16x16x32_bf16 v[8:11], v[154:157], v[162:165], v[8:11]
	v_mfma_f32_16x16x32_bf16 v[60:63], v[150:153], v[190:193], v[60:63]
	v_mfma_f32_16x16x32_bf16 v[56:59], v[158:161], v[190:193], v[56:59]
	v_mfma_f32_16x16x32_bf16 v[44:47], v[150:153], v[182:185], v[44:47]
	v_mfma_f32_16x16x32_bf16 v[40:43], v[158:161], v[182:185], v[40:43]
	v_mfma_f32_16x16x32_bf16 v[28:31], v[150:153], v[174:177], v[28:31]
	v_mfma_f32_16x16x32_bf16 v[24:27], v[158:161], v[174:177], v[24:27]
	v_mfma_f32_16x16x32_bf16 v[12:15], v[150:153], v[166:169], v[12:15]
	v_mfma_f32_16x16x32_bf16 v[8:11], v[158:161], v[166:169], v[8:11]
	v_mfma_f32_16x16x32_bf16 v[52:55], v[130:133], v[186:189], v[52:55]
	v_mfma_f32_16x16x32_bf16 v[48:51], v[138:141], v[186:189], v[48:51]
	v_mfma_f32_16x16x32_bf16 v[36:39], v[130:133], v[178:181], v[36:39]
	v_mfma_f32_16x16x32_bf16 v[32:35], v[138:141], v[178:181], v[32:35]
	v_mfma_f32_16x16x32_bf16 v[20:23], v[130:133], v[170:173], v[20:23]
	v_mfma_f32_16x16x32_bf16 v[16:19], v[138:141], v[170:173], v[16:19]
	v_mfma_f32_16x16x32_bf16 v[4:7], v[130:133], v[162:165], v[4:7]
	v_mfma_f32_16x16x32_bf16 v[0:3], v[138:141], v[162:165], v[0:3]
	v_mfma_f32_16x16x32_bf16 v[52:55], v[134:137], v[190:193], v[52:55]
	v_mfma_f32_16x16x32_bf16 v[48:51], v[142:145], v[190:193], v[48:51]
	v_mfma_f32_16x16x32_bf16 v[36:39], v[134:137], v[182:185], v[36:39]
	v_mfma_f32_16x16x32_bf16 v[32:35], v[142:145], v[182:185], v[32:35]
	v_mfma_f32_16x16x32_bf16 v[20:23], v[134:137], v[174:177], v[20:23]
	v_mfma_f32_16x16x32_bf16 v[16:19], v[142:145], v[174:177], v[16:19]
	v_mfma_f32_16x16x32_bf16 v[4:7], v[134:137], v[166:169], v[4:7]
	v_mfma_f32_16x16x32_bf16 v[0:3], v[142:145], v[166:169], v[0:3]
.LBB0_516:
	s_barrier
	s_add_i32 vcc_lo, 0, 0x18000
	s_add_i32 vcc_hi, 0, 0x1c000
	v_add_u32_e32 v130, vcc_lo, v223
	v_add_u32_e32 v142, vcc_hi, v223
	ds_read_b128 v[146:149], v130
	ds_read_b128 v[150:153], v130 offset:1024
	ds_read_b128 v[154:157], v130 offset:2048
	ds_read_b128 v[158:161], v130 offset:3072
	ds_read_b128 v[130:133], v142
	ds_read_b128 v[134:137], v142 offset:1024
	ds_read_b128 v[138:141], v142 offset:2048
	ds_read_b128 v[142:145], v142 offset:3072
	s_and_b64 s[26:27], s[26:27], exec
	s_cselect_b32 s27, s72, s86
	s_cselect_b32 s26, 0, s87
	s_add_u32 s24, s24, s27
	s_addc_u32 s25, s25, s26
	s_mov_b32 m0, s89
	v_lshl_add_u64 v[226:227], s[24:25], 0, v[198:199]
	ds_read_b128 v[162:165], v224 offset:32768
	ds_read_b128 v[166:169], v224 offset:33792
	ds_read_b128 v[170:173], v224 offset:34816
	ds_read_b128 v[174:177], v224 offset:35840
	ds_read_b128 v[178:181], v224 offset:36864
	ds_read_b128 v[182:185], v224 offset:37888
	ds_read_b128 v[186:189], v224 offset:38912
	ds_read_b128 v[190:193], v224 offset:39936
	global_load_lds_dwordx4 v[226:227], off
	s_mov_b32 m0, s90
	v_lshl_add_u64 v[226:227], s[24:25], 0, v[202:203]
	global_load_lds_dwordx4 v[226:227], off
	s_waitcnt vmcnt(8) lgkmcnt(0)
	s_barrier
	v_mfma_f32_16x16x32_bf16 v[124:127], v[146:149], v[162:165], v[124:127]
	v_mfma_f32_16x16x32_bf16 v[120:123], v[154:157], v[162:165], v[120:123]
	v_mfma_f32_16x16x32_bf16 v[116:119], v[146:149], v[170:173], v[116:119]
	v_mfma_f32_16x16x32_bf16 v[108:111], v[154:157], v[170:173], v[108:111]
	v_mfma_f32_16x16x32_bf16 v[100:103], v[146:149], v[178:181], v[100:103]
	v_mfma_f32_16x16x32_bf16 v[92:95], v[154:157], v[178:181], v[92:95]
	v_mfma_f32_16x16x32_bf16 v[84:87], v[146:149], v[186:189], v[84:87]
	v_mfma_f32_16x16x32_bf16 v[76:79], v[154:157], v[186:189], v[76:79]
	v_mfma_f32_16x16x32_bf16 v[124:127], v[150:153], v[166:169], v[124:127]
	v_mfma_f32_16x16x32_bf16 v[120:123], v[158:161], v[166:169], v[120:123]
	v_mfma_f32_16x16x32_bf16 v[116:119], v[150:153], v[174:177], v[116:119]
	v_mfma_f32_16x16x32_bf16 v[108:111], v[158:161], v[174:177], v[108:111]
	v_mfma_f32_16x16x32_bf16 v[100:103], v[150:153], v[182:185], v[100:103]
	v_mfma_f32_16x16x32_bf16 v[92:95], v[158:161], v[182:185], v[92:95]
	v_mfma_f32_16x16x32_bf16 v[84:87], v[150:153], v[190:193], v[84:87]
	v_mfma_f32_16x16x32_bf16 v[76:79], v[158:161], v[190:193], v[76:79]
	v_mfma_f32_16x16x32_bf16 v[112:115], v[130:133], v[162:165], v[112:115]
	v_mfma_f32_16x16x32_bf16 v[104:107], v[138:141], v[162:165], v[104:107]
	v_mfma_f32_16x16x32_bf16 v[96:99], v[130:133], v[170:173], v[96:99]
	v_mfma_f32_16x16x32_bf16 v[88:91], v[138:141], v[170:173], v[88:91]
	v_mfma_f32_16x16x32_bf16 v[80:83], v[130:133], v[178:181], v[80:83]
	v_mfma_f32_16x16x32_bf16 v[72:75], v[138:141], v[178:181], v[72:75]
	v_mfma_f32_16x16x32_bf16 v[68:71], v[130:133], v[186:189], v[68:71]
	v_mfma_f32_16x16x32_bf16 v[64:67], v[138:141], v[186:189], v[64:67]
	v_mfma_f32_16x16x32_bf16 v[112:115], v[134:137], v[166:169], v[112:115]
	v_mfma_f32_16x16x32_bf16 v[104:107], v[142:145], v[166:169], v[104:107]
	v_mfma_f32_16x16x32_bf16 v[96:99], v[134:137], v[174:177], v[96:99]
	v_mfma_f32_16x16x32_bf16 v[88:91], v[142:145], v[174:177], v[88:91]
	v_mfma_f32_16x16x32_bf16 v[80:83], v[134:137], v[182:185], v[80:83]
	v_mfma_f32_16x16x32_bf16 v[72:75], v[142:145], v[182:185], v[72:75]
	v_mfma_f32_16x16x32_bf16 v[68:71], v[134:137], v[190:193], v[68:71]
	v_mfma_f32_16x16x32_bf16 v[64:67], v[142:145], v[190:193], v[64:67]
	s_barrier
	s_add_i32 s24, vcc_lo, s28
	v_lshl_add_u64 v[214:215], v[214:215], 0, s[42:43]
	s_mov_b32 m0, s24
	ds_read_b128 v[186:189], v224 offset:49152
	ds_read_b128 v[190:193], v224 offset:50176
	ds_read_b128 v[178:181], v224 offset:51200
	ds_read_b128 v[182:185], v224 offset:52224
	ds_read_b128 v[170:173], v224 offset:53248
	ds_read_b128 v[174:177], v224 offset:54272
	ds_read_b128 v[162:165], v224 offset:55296
	ds_read_b128 v[166:169], v224 offset:56320
	global_load_lds_dwordx4 v[214:215], off
	s_add_i32 m0, s24, 0x2000
	s_add_u32 s22, s22, 0x80080
	v_lshl_add_u64 v[214:215], v[216:217], 0, s[42:43]
	s_addc_u32 s23, s23, 0
	s_add_i32 s24, vcc_hi, s28
	global_load_lds_dwordx4 v[214:215], off
	v_lshl_add_u64 v[214:215], s[22:23], 0, v[200:201]
	s_mov_b32 m0, s24
	s_and_b64 vcc, exec, s[58:59]
	global_load_lds_dwordx4 v[214:215], off
	s_add_i32 m0, s24, 0x2000
	v_lshl_add_u64 v[214:215], s[22:23], 0, v[204:205]
	global_load_lds_dwordx4 v[214:215], off
	s_mov_b32 m0, s91
	v_lshl_add_u64 v[214:215], v[218:219], 0, s[42:43]
	global_load_lds_dwordx4 v[214:215], off
	s_mov_b32 m0, s94
	v_lshl_add_u64 v[214:215], v[220:221], 0, s[42:43]
	global_load_lds_dwordx4 v[214:215], off
	s_waitcnt vmcnt(8) lgkmcnt(0)
	s_barrier
	s_cbranch_vccnz .LBB0_513
	s_waitcnt lgkmcnt(0)
	v_mfma_f32_16x16x32_bf16 v[60:63], v[146:149], v[186:189], v[60:63]
	v_mfma_f32_16x16x32_bf16 v[56:59], v[154:157], v[186:189], v[56:59]
	v_mfma_f32_16x16x32_bf16 v[44:47], v[146:149], v[178:181], v[44:47]
	v_mfma_f32_16x16x32_bf16 v[40:43], v[154:157], v[178:181], v[40:43]
	v_mfma_f32_16x16x32_bf16 v[28:31], v[146:149], v[170:173], v[28:31]
	v_mfma_f32_16x16x32_bf16 v[24:27], v[154:157], v[170:173], v[24:27]
	v_mfma_f32_16x16x32_bf16 v[12:15], v[146:149], v[162:165], v[12:15]
	v_mfma_f32_16x16x32_bf16 v[8:11], v[154:157], v[162:165], v[8:11]
	v_mfma_f32_16x16x32_bf16 v[60:63], v[150:153], v[190:193], v[60:63]
	v_mfma_f32_16x16x32_bf16 v[56:59], v[158:161], v[190:193], v[56:59]
	v_mfma_f32_16x16x32_bf16 v[44:47], v[150:153], v[182:185], v[44:47]
	v_mfma_f32_16x16x32_bf16 v[40:43], v[158:161], v[182:185], v[40:43]
	v_mfma_f32_16x16x32_bf16 v[28:31], v[150:153], v[174:177], v[28:31]
	v_mfma_f32_16x16x32_bf16 v[24:27], v[158:161], v[174:177], v[24:27]
	v_mfma_f32_16x16x32_bf16 v[12:15], v[150:153], v[166:169], v[12:15]
	v_mfma_f32_16x16x32_bf16 v[8:11], v[158:161], v[166:169], v[8:11]
	v_mfma_f32_16x16x32_bf16 v[52:55], v[130:133], v[186:189], v[52:55]
	v_mfma_f32_16x16x32_bf16 v[48:51], v[138:141], v[186:189], v[48:51]
	v_mfma_f32_16x16x32_bf16 v[36:39], v[130:133], v[178:181], v[36:39]
	v_mfma_f32_16x16x32_bf16 v[32:35], v[138:141], v[178:181], v[32:35]
	v_mfma_f32_16x16x32_bf16 v[20:23], v[130:133], v[170:173], v[20:23]
	v_mfma_f32_16x16x32_bf16 v[16:19], v[138:141], v[170:173], v[16:19]
	v_mfma_f32_16x16x32_bf16 v[4:7], v[130:133], v[162:165], v[4:7]
	v_mfma_f32_16x16x32_bf16 v[0:3], v[138:141], v[162:165], v[0:3]
	v_mfma_f32_16x16x32_bf16 v[52:55], v[134:137], v[190:193], v[52:55]
	v_mfma_f32_16x16x32_bf16 v[48:51], v[142:145], v[190:193], v[48:51]
	v_mfma_f32_16x16x32_bf16 v[36:39], v[134:137], v[182:185], v[36:39]
	v_mfma_f32_16x16x32_bf16 v[32:35], v[142:145], v[182:185], v[32:35]
	v_mfma_f32_16x16x32_bf16 v[20:23], v[134:137], v[174:177], v[20:23]
	v_mfma_f32_16x16x32_bf16 v[16:19], v[142:145], v[174:177], v[16:19]
	v_mfma_f32_16x16x32_bf16 v[4:7], v[134:137], v[166:169], v[4:7]
	v_mfma_f32_16x16x32_bf16 v[0:3], v[142:145], v[166:169], v[0:3]
	s_branch .LBB0_513

.LBB0_725:
	s_add_u32 s2, s64, 0xfffe0080
	s_addc_u32 s3, s65, -1
	s_add_i32 s29, 0, 0x10000
	s_cmp_eq_u32 s66, 4
	s_cselect_b32 s25, s61, s3
	s_cselect_b32 s24, s60, s2
	v_add_u32_e32 v145, s29, v143
	s_cselect_b32 s23, s63, s17
	s_cselect_b32 s22, s62, s15
	s_add_i32 s30, 0, 0x14000
	ds_read_b128 v[146:149], v145
	ds_read_b128 v[150:153], v145 offset:1024
	ds_read_b128 v[154:157], v145 offset:2048
	ds_read_b128 v[158:161], v145 offset:3072
	v_add_u32_e32 v145, s30, v143
	ds_read_b128 v[162:165], v145
	ds_read_b128 v[166:169], v145 offset:1024
	ds_read_b128 v[170:173], v145 offset:2048
	ds_read_b128 v[174:177], v145 offset:3072
	v_lshl_add_u64 v[214:215], s[64:65], 0, v[138:139]
	s_add_i32 m0, s53, 0xc000
	ds_read_b128 v[178:181], v144
	ds_read_b128 v[182:185], v144 offset:1024
	ds_read_b128 v[186:189], v144 offset:2048
	ds_read_b128 v[190:193], v144 offset:3072
	ds_read_b128 v[198:201], v144 offset:4096
	ds_read_b128 v[202:205], v144 offset:5120
	ds_read_b128 v[206:209], v144 offset:6144
	ds_read_b128 v[210:213], v144 offset:7168
	global_load_lds_dwordx4 v[214:215], off
	s_add_i32 m0, s53, 0xe000
	v_lshl_add_u64 v[214:215], s[64:65], 0, v[140:141]
	global_load_lds_dwordx4 v[214:215], off
	s_waitcnt vmcnt(8) lgkmcnt(0)
	s_barrier
	v_mfma_f32_16x16x32_bf16 v[124:127], v[146:149], v[178:181], v[124:127]
	v_mfma_f32_16x16x32_bf16 v[120:123], v[154:157], v[178:181], v[120:123]
	v_mfma_f32_16x16x32_bf16 v[116:119], v[146:149], v[186:189], v[116:119]
	v_mfma_f32_16x16x32_bf16 v[108:111], v[154:157], v[186:189], v[108:111]
	v_mfma_f32_16x16x32_bf16 v[100:103], v[146:149], v[198:201], v[100:103]
	v_mfma_f32_16x16x32_bf16 v[92:95], v[154:157], v[198:201], v[92:95]
	v_mfma_f32_16x16x32_bf16 v[84:87], v[146:149], v[206:209], v[84:87]
	v_mfma_f32_16x16x32_bf16 v[76:79], v[154:157], v[206:209], v[76:79]
	v_mfma_f32_16x16x32_bf16 v[124:127], v[150:153], v[182:185], v[124:127]
	v_mfma_f32_16x16x32_bf16 v[120:123], v[158:161], v[182:185], v[120:123]
	v_mfma_f32_16x16x32_bf16 v[116:119], v[150:153], v[190:193], v[116:119]
	v_mfma_f32_16x16x32_bf16 v[108:111], v[158:161], v[190:193], v[108:111]
	v_mfma_f32_16x16x32_bf16 v[100:103], v[150:153], v[202:205], v[100:103]
	v_mfma_f32_16x16x32_bf16 v[92:95], v[158:161], v[202:205], v[92:95]
	v_mfma_f32_16x16x32_bf16 v[84:87], v[150:153], v[210:213], v[84:87]
	v_mfma_f32_16x16x32_bf16 v[76:79], v[158:161], v[210:213], v[76:79]
	v_mfma_f32_16x16x32_bf16 v[112:115], v[162:165], v[178:181], v[112:115]
	v_mfma_f32_16x16x32_bf16 v[104:107], v[170:173], v[178:181], v[104:107]
	v_mfma_f32_16x16x32_bf16 v[96:99], v[162:165], v[186:189], v[96:99]
	v_mfma_f32_16x16x32_bf16 v[88:91], v[170:173], v[186:189], v[88:91]
	v_mfma_f32_16x16x32_bf16 v[80:83], v[162:165], v[198:201], v[80:83]
	v_mfma_f32_16x16x32_bf16 v[72:75], v[170:173], v[198:201], v[72:75]
	v_mfma_f32_16x16x32_bf16 v[68:71], v[162:165], v[206:209], v[68:71]
	v_mfma_f32_16x16x32_bf16 v[64:67], v[170:173], v[206:209], v[64:67]
	v_mfma_f32_16x16x32_bf16 v[112:115], v[166:169], v[182:185], v[112:115]
	v_mfma_f32_16x16x32_bf16 v[104:107], v[174:177], v[182:185], v[104:107]
	v_mfma_f32_16x16x32_bf16 v[96:99], v[166:169], v[190:193], v[96:99]
	v_mfma_f32_16x16x32_bf16 v[88:91], v[174:177], v[190:193], v[88:91]
	v_mfma_f32_16x16x32_bf16 v[80:83], v[166:169], v[202:205], v[80:83]
	v_mfma_f32_16x16x32_bf16 v[72:75], v[174:177], v[202:205], v[72:75]
	v_mfma_f32_16x16x32_bf16 v[68:71], v[166:169], v[210:213], v[68:71]
	v_mfma_f32_16x16x32_bf16 v[64:67], v[174:177], v[210:213], v[64:67]
	s_barrier
	s_add_i32 s2, s29, s39
	v_lshl_add_u64 v[214:215], s[22:23], 0, v[134:135]
	s_mov_b32 m0, s2
	ds_read_b128 v[178:181], v144 offset:16384
	ds_read_b128 v[182:185], v144 offset:17408
	ds_read_b128 v[186:189], v144 offset:18432
	ds_read_b128 v[190:193], v144 offset:19456
	ds_read_b128 v[198:201], v144 offset:20480
	ds_read_b128 v[202:205], v144 offset:21504
	ds_read_b128 v[206:209], v144 offset:22528
	ds_read_b128 v[210:213], v144 offset:23552
	global_load_lds_dwordx4 v[214:215], off
	s_add_i32 m0, s2, 0x2000
	s_add_u32 s2, s22, 0x20000
	v_lshl_add_u64 v[216:217], s[22:23], 0, v[130:131]
	s_addc_u32 s3, s23, 0
	s_add_i32 s29, s30, s39
	global_load_lds_dwordx4 v[216:217], off
	v_lshl_add_u64 v[218:219], s[2:3], 0, v[134:135]
	s_mov_b32 m0, s29
	v_lshl_add_u64 v[220:221], s[24:25], 0, v[132:133]
	global_load_lds_dwordx4 v[218:219], off
	s_add_i32 m0, s29, 0x2000
	v_lshl_add_u64 v[218:219], s[2:3], 0, v[130:131]
	global_load_lds_dwordx4 v[218:219], off
	s_mov_b32 m0, s53
	v_lshl_add_u64 v[218:219], s[24:25], 0, v[136:137]
	global_load_lds_dwordx4 v[218:219], off
	s_mov_b32 m0, s68
	s_nop 0
	global_load_lds_dwordx4 v[220:221], off
	s_waitcnt vmcnt(8) lgkmcnt(0)
	s_barrier
	v_mfma_f32_16x16x32_bf16 v[60:63], v[146:149], v[178:181], v[60:63]
	v_mfma_f32_16x16x32_bf16 v[56:59], v[154:157], v[178:181], v[56:59]
	v_mfma_f32_16x16x32_bf16 v[52:55], v[146:149], v[186:189], v[52:55]
	v_mfma_f32_16x16x32_bf16 v[44:47], v[154:157], v[186:189], v[44:47]
	v_mfma_f32_16x16x32_bf16 v[36:39], v[146:149], v[198:201], v[36:39]
	v_mfma_f32_16x16x32_bf16 v[28:31], v[154:157], v[198:201], v[28:31]
	v_mfma_f32_16x16x32_bf16 v[20:23], v[146:149], v[206:209], v[20:23]
	v_mfma_f32_16x16x32_bf16 v[12:15], v[154:157], v[206:209], v[12:15]
	v_mfma_f32_16x16x32_bf16 v[60:63], v[150:153], v[182:185], v[60:63]
	v_mfma_f32_16x16x32_bf16 v[56:59], v[158:161], v[182:185], v[56:59]
	v_mfma_f32_16x16x32_bf16 v[52:55], v[150:153], v[190:193], v[52:55]
	v_mfma_f32_16x16x32_bf16 v[44:47], v[158:161], v[190:193], v[44:47]
	v_mfma_f32_16x16x32_bf16 v[36:39], v[150:153], v[202:205], v[36:39]
	v_mfma_f32_16x16x32_bf16 v[28:31], v[158:161], v[202:205], v[28:31]
	v_mfma_f32_16x16x32_bf16 v[20:23], v[150:153], v[210:213], v[20:23]
	v_mfma_f32_16x16x32_bf16 v[12:15], v[158:161], v[210:213], v[12:15]
	v_mfma_f32_16x16x32_bf16 v[48:51], v[162:165], v[178:181], v[48:51]
	v_mfma_f32_16x16x32_bf16 v[40:43], v[170:173], v[178:181], v[40:43]
	v_mfma_f32_16x16x32_bf16 v[32:35], v[162:165], v[186:189], v[32:35]
	v_mfma_f32_16x16x32_bf16 v[24:27], v[170:173], v[186:189], v[24:27]
	v_mfma_f32_16x16x32_bf16 v[16:19], v[162:165], v[198:201], v[16:19]
	v_mfma_f32_16x16x32_bf16 v[8:11], v[170:173], v[198:201], v[8:11]
	v_mfma_f32_16x16x32_bf16 v[4:7], v[162:165], v[206:209], v[4:7]
	v_mfma_f32_16x16x32_bf16 v[0:3], v[170:173], v[206:209], v[0:3]
	v_mfma_f32_16x16x32_bf16 v[48:51], v[166:169], v[182:185], v[48:51]
	v_mfma_f32_16x16x32_bf16 v[40:43], v[174:177], v[182:185], v[40:43]
	v_mfma_f32_16x16x32_bf16 v[32:35], v[166:169], v[190:193], v[32:35]
	v_mfma_f32_16x16x32_bf16 v[24:27], v[174:177], v[190:193], v[24:27]
	v_mfma_f32_16x16x32_bf16 v[16:19], v[166:169], v[202:205], v[16:19]
	v_mfma_f32_16x16x32_bf16 v[8:11], v[174:177], v[202:205], v[8:11]
	v_mfma_f32_16x16x32_bf16 v[4:7], v[166:169], v[210:213], v[4:7]
	v_mfma_f32_16x16x32_bf16 v[0:3], v[174:177], v[210:213], v[0:3]
	s_barrier
	s_add_i32 s29, 0, 0x18000
	v_add_u32_e32 v145, s29, v143
	s_add_i32 s30, 0, 0x1c000
	ds_read_b128 v[146:149], v145
	ds_read_b128 v[150:153], v145 offset:1024
	ds_read_b128 v[154:157], v145 offset:2048
	ds_read_b128 v[158:161], v145 offset:3072
	v_add_u32_e32 v145, s30, v143
	ds_read_b128 v[162:165], v145
	ds_read_b128 v[166:169], v145 offset:1024
	ds_read_b128 v[170:173], v145 offset:2048
	ds_read_b128 v[174:177], v145 offset:3072
	s_add_u32 s2, s24, 0x20000
	s_addc_u32 s3, s25, 0
	s_mov_b32 m0, s69
	v_lshl_add_u64 v[222:223], s[2:3], 0, v[136:137]
	ds_read_b128 v[178:181], v144 offset:32768
	ds_read_b128 v[182:185], v144 offset:33792
	ds_read_b128 v[186:189], v144 offset:34816
	ds_read_b128 v[190:193], v144 offset:35840
	ds_read_b128 v[198:201], v144 offset:36864
	ds_read_b128 v[202:205], v144 offset:37888
	ds_read_b128 v[206:209], v144 offset:38912
	ds_read_b128 v[210:213], v144 offset:39936
	global_load_lds_dwordx4 v[222:223], off
	s_mov_b32 m0, s70
	v_lshl_add_u64 v[222:223], s[2:3], 0, v[132:133]
	global_load_lds_dwordx4 v[222:223], off
	s_waitcnt vmcnt(8) lgkmcnt(0)
	s_barrier
	v_mfma_f32_16x16x32_bf16 v[124:127], v[146:149], v[178:181], v[124:127]
	v_mfma_f32_16x16x32_bf16 v[120:123], v[154:157], v[178:181], v[120:123]
	v_mfma_f32_16x16x32_bf16 v[116:119], v[146:149], v[186:189], v[116:119]
	v_mfma_f32_16x16x32_bf16 v[108:111], v[154:157], v[186:189], v[108:111]
	v_mfma_f32_16x16x32_bf16 v[100:103], v[146:149], v[198:201], v[100:103]
	v_mfma_f32_16x16x32_bf16 v[92:95], v[154:157], v[198:201], v[92:95]
	v_mfma_f32_16x16x32_bf16 v[84:87], v[146:149], v[206:209], v[84:87]
	v_mfma_f32_16x16x32_bf16 v[76:79], v[154:157], v[206:209], v[76:79]
	v_mfma_f32_16x16x32_bf16 v[124:127], v[150:153], v[182:185], v[124:127]
	v_mfma_f32_16x16x32_bf16 v[120:123], v[158:161], v[182:185], v[120:123]
	v_mfma_f32_16x16x32_bf16 v[116:119], v[150:153], v[190:193], v[116:119]
	v_mfma_f32_16x16x32_bf16 v[108:111], v[158:161], v[190:193], v[108:111]
	v_mfma_f32_16x16x32_bf16 v[100:103], v[150:153], v[202:205], v[100:103]
	v_mfma_f32_16x16x32_bf16 v[92:95], v[158:161], v[202:205], v[92:95]
	v_mfma_f32_16x16x32_bf16 v[84:87], v[150:153], v[210:213], v[84:87]
	v_mfma_f32_16x16x32_bf16 v[76:79], v[158:161], v[210:213], v[76:79]
	v_mfma_f32_16x16x32_bf16 v[112:115], v[162:165], v[178:181], v[112:115]
	v_mfma_f32_16x16x32_bf16 v[104:107], v[170:173], v[178:181], v[104:107]
	v_mfma_f32_16x16x32_bf16 v[96:99], v[162:165], v[186:189], v[96:99]
	v_mfma_f32_16x16x32_bf16 v[88:91], v[170:173], v[186:189], v[88:91]
	v_mfma_f32_16x16x32_bf16 v[80:83], v[162:165], v[198:201], v[80:83]
	v_mfma_f32_16x16x32_bf16 v[72:75], v[170:173], v[198:201], v[72:75]
	v_mfma_f32_16x16x32_bf16 v[68:71], v[162:165], v[206:209], v[68:71]
	v_mfma_f32_16x16x32_bf16 v[64:67], v[170:173], v[206:209], v[64:67]
	v_mfma_f32_16x16x32_bf16 v[112:115], v[166:169], v[182:185], v[112:115]
	v_mfma_f32_16x16x32_bf16 v[104:107], v[174:177], v[182:185], v[104:107]
	v_mfma_f32_16x16x32_bf16 v[96:99], v[166:169], v[190:193], v[96:99]
	v_mfma_f32_16x16x32_bf16 v[88:91], v[174:177], v[190:193], v[88:91]
	v_mfma_f32_16x16x32_bf16 v[80:83], v[166:169], v[202:205], v[80:83]
	v_mfma_f32_16x16x32_bf16 v[72:75], v[174:177], v[202:205], v[72:75]
	v_mfma_f32_16x16x32_bf16 v[68:71], v[166:169], v[210:213], v[68:71]
	v_mfma_f32_16x16x32_bf16 v[64:67], v[174:177], v[210:213], v[64:67]
	s_barrier
	s_add_i32 s2, s29, s39
	v_lshl_add_u64 v[214:215], v[214:215], 0, s[42:43]
	s_mov_b32 m0, s2
	ds_read_b128 v[178:181], v144 offset:49152
	ds_read_b128 v[182:185], v144 offset:50176
	ds_read_b128 v[186:189], v144 offset:51200
	ds_read_b128 v[190:193], v144 offset:52224
	ds_read_b128 v[198:201], v144 offset:53248
	ds_read_b128 v[202:205], v144 offset:54272
	ds_read_b128 v[206:209], v144 offset:55296
	ds_read_b128 v[210:213], v144 offset:56320
	global_load_lds_dwordx4 v[214:215], off
	s_add_i32 m0, s2, 0x2000
	s_add_u32 s2, s22, 0x20080
	v_lshl_add_u64 v[214:215], v[216:217], 0, s[42:43]
	s_addc_u32 s3, s23, 0
	s_add_i32 s22, s30, s39
	global_load_lds_dwordx4 v[214:215], off
	s_mov_b32 m0, s22
	v_lshl_add_u64 v[214:215], s[2:3], 0, v[134:135]
	global_load_lds_dwordx4 v[214:215], off
	s_add_i32 m0, s22, 0x2000
	v_lshl_add_u64 v[214:215], s[2:3], 0, v[130:131]
	global_load_lds_dwordx4 v[214:215], off
	s_mov_b32 m0, s71
	v_lshl_add_u64 v[214:215], v[218:219], 0, s[42:43]
	global_load_lds_dwordx4 v[214:215], off
	s_mov_b32 m0, s74
	v_lshl_add_u64 v[214:215], v[220:221], 0, s[42:43]
	global_load_lds_dwordx4 v[214:215], off
	s_waitcnt vmcnt(8) lgkmcnt(0)
	s_barrier
	v_mfma_f32_16x16x32_bf16 v[60:63], v[146:149], v[178:181], v[60:63]
	v_mfma_f32_16x16x32_bf16 v[56:59], v[154:157], v[178:181], v[56:59]
	v_mfma_f32_16x16x32_bf16 v[52:55], v[146:149], v[186:189], v[52:55]
	v_mfma_f32_16x16x32_bf16 v[44:47], v[154:157], v[186:189], v[44:47]
	v_mfma_f32_16x16x32_bf16 v[36:39], v[146:149], v[198:201], v[36:39]
	v_mfma_f32_16x16x32_bf16 v[28:31], v[154:157], v[198:201], v[28:31]
	v_mfma_f32_16x16x32_bf16 v[20:23], v[146:149], v[206:209], v[20:23]
	v_mfma_f32_16x16x32_bf16 v[12:15], v[154:157], v[206:209], v[12:15]
	v_mfma_f32_16x16x32_bf16 v[60:63], v[150:153], v[182:185], v[60:63]
	v_mfma_f32_16x16x32_bf16 v[56:59], v[158:161], v[182:185], v[56:59]
	v_mfma_f32_16x16x32_bf16 v[52:55], v[150:153], v[190:193], v[52:55]
	v_mfma_f32_16x16x32_bf16 v[44:47], v[158:161], v[190:193], v[44:47]
	v_mfma_f32_16x16x32_bf16 v[36:39], v[150:153], v[202:205], v[36:39]
	v_mfma_f32_16x16x32_bf16 v[28:31], v[158:161], v[202:205], v[28:31]
	v_mfma_f32_16x16x32_bf16 v[20:23], v[150:153], v[210:213], v[20:23]
	v_mfma_f32_16x16x32_bf16 v[12:15], v[158:161], v[210:213], v[12:15]
	v_mfma_f32_16x16x32_bf16 v[48:51], v[162:165], v[178:181], v[48:51]
	v_mfma_f32_16x16x32_bf16 v[40:43], v[170:173], v[178:181], v[40:43]
	v_mfma_f32_16x16x32_bf16 v[32:35], v[162:165], v[186:189], v[32:35]
	v_mfma_f32_16x16x32_bf16 v[24:27], v[170:173], v[186:189], v[24:27]
	v_mfma_f32_16x16x32_bf16 v[16:19], v[162:165], v[198:201], v[16:19]
	v_mfma_f32_16x16x32_bf16 v[8:11], v[170:173], v[198:201], v[8:11]
	v_mfma_f32_16x16x32_bf16 v[4:7], v[162:165], v[206:209], v[4:7]
	v_mfma_f32_16x16x32_bf16 v[0:3], v[170:173], v[206:209], v[0:3]
	v_mfma_f32_16x16x32_bf16 v[48:51], v[166:169], v[182:185], v[48:51]
	v_mfma_f32_16x16x32_bf16 v[40:43], v[174:177], v[182:185], v[40:43]
	v_mfma_f32_16x16x32_bf16 v[32:35], v[166:169], v[190:193], v[32:35]
	v_mfma_f32_16x16x32_bf16 v[24:27], v[174:177], v[190:193], v[24:27]
	v_mfma_f32_16x16x32_bf16 v[16:19], v[166:169], v[202:205], v[16:19]
	v_mfma_f32_16x16x32_bf16 v[8:11], v[174:177], v[202:205], v[8:11]
	v_mfma_f32_16x16x32_bf16 v[4:7], v[166:169], v[210:213], v[4:7]
	v_mfma_f32_16x16x32_bf16 v[0:3], v[174:177], v[210:213], v[0:3]
	s_barrier
	s_add_i32 s66, s66, 2
	s_add_u32 s64, s64, 0x100
	s_addc_u32 s65, s65, 0
	s_add_u32 s15, s15, 0x100
	s_addc_u32 s17, s17, 0
	s_cmp_gt_u32 s66, 5
	s_cbranch_scc0 .LBB0_725
	s_and_b64 vcc, exec, s[10:11]
	s_cbranch_vccz .LBB0_728
	s_barrier

.LBB0_969:
	s_add_u32 s24, s18, s92
	s_addc_u32 s25, s19, s93
	s_add_u32 s60, s24, 0x100
	s_addc_u32 s61, s25, 0
	s_add_u32 s81, s2, s92
	s_addc_u32 s84, s29, s93
	s_add_i32 vcc_lo, 0, 0x10000
	s_cmpk_eq_i32 s92, 0xf00
	s_cselect_b64 s[26:27], -1, 0
	s_and_b64 s[24:25], s[26:27], exec
	s_cselect_b32 s25, s15, s61
	s_cselect_b32 s24, s17, s60
	s_waitcnt lgkmcnt(0)
	v_add_u32_e32 v104, vcc_lo, v234
	s_cselect_b32 s85, s67, s84
	s_cselect_b32 s84, s3, s81
	s_add_i32 s81, 0, 0x14000
	ds_read_b128 v[162:165], v104
	ds_read_b128 v[166:169], v104 offset:1024
	ds_read_b128 v[170:173], v104 offset:2048
	ds_read_b128 v[174:177], v104 offset:3072
	v_add_u32_e32 v104, s81, v234
	ds_read_b128 v[146:149], v104
	ds_read_b128 v[150:153], v104 offset:1024
	ds_read_b128 v[154:157], v104 offset:2048
	ds_read_b128 v[158:161], v104 offset:3072
	v_lshl_add_u64 v[104:105], v[208:209], 0, s[92:93]
	s_add_i32 m0, s53, 0xc000
	ds_read_b128 v[178:181], v236
	ds_read_b128 v[182:185], v236 offset:1024
	ds_read_b128 v[186:189], v236 offset:2048
	ds_read_b128 v[190:193], v236 offset:3072
	ds_read_b128 v[210:213], v236 offset:4096
	ds_read_b128 v[214:217], v236 offset:5120
	ds_read_b128 v[218:221], v236 offset:6144
	ds_read_b128 v[222:225], v236 offset:7168
	global_load_lds_dwordx4 v[104:105], off
	s_add_i32 m0, s53, 0xe000
	v_lshl_add_u64 v[104:105], v[206:207], 0, s[92:93]
	global_load_lds_dwordx4 v[104:105], off
	s_waitcnt vmcnt(8) lgkmcnt(0)
	s_barrier
	v_mfma_f32_16x16x32_bf16 v[104:107], v[162:165], v[178:181], v[142:145]
	v_mfma_f32_16x16x32_bf16 v[108:111], v[170:173], v[178:181], v[138:141]
	v_mfma_f32_16x16x32_bf16 v[116:119], v[162:165], v[186:189], v[120:123]
	v_mfma_f32_16x16x32_bf16 v[112:115], v[170:173], v[186:189], v[112:115]
	v_mfma_f32_16x16x32_bf16 v[92:95], v[162:165], v[210:213], v[92:95]
	v_mfma_f32_16x16x32_bf16 v[88:91], v[170:173], v[210:213], v[88:91]
	v_mfma_f32_16x16x32_bf16 v[76:79], v[162:165], v[218:221], v[76:79]
	v_mfma_f32_16x16x32_bf16 v[72:75], v[170:173], v[218:221], v[72:75]
	v_mfma_f32_16x16x32_bf16 v[104:107], v[166:169], v[182:185], v[104:107]
	v_mfma_f32_16x16x32_bf16 v[108:111], v[174:177], v[182:185], v[108:111]
	v_mfma_f32_16x16x32_bf16 v[116:119], v[166:169], v[190:193], v[116:119]
	v_mfma_f32_16x16x32_bf16 v[112:115], v[174:177], v[190:193], v[112:115]
	v_mfma_f32_16x16x32_bf16 v[92:95], v[166:169], v[214:217], v[92:95]
	v_mfma_f32_16x16x32_bf16 v[88:91], v[174:177], v[214:217], v[88:91]
	v_mfma_f32_16x16x32_bf16 v[76:79], v[166:169], v[222:225], v[76:79]
	v_mfma_f32_16x16x32_bf16 v[72:75], v[174:177], v[222:225], v[72:75]
	v_mfma_f32_16x16x32_bf16 v[120:123], v[146:149], v[178:181], v[134:137]
	v_mfma_f32_16x16x32_bf16 v[130:133], v[150:153], v[182:185], v[120:123]
	v_mfma_f32_16x16x32_bf16 v[120:123], v[154:157], v[178:181], v[124:127]
	v_mfma_f32_16x16x32_bf16 v[100:103], v[146:149], v[186:189], v[100:103]
	v_mfma_f32_16x16x32_bf16 v[96:99], v[154:157], v[186:189], v[96:99]
	v_mfma_f32_16x16x32_bf16 v[84:87], v[146:149], v[210:213], v[84:87]
	v_mfma_f32_16x16x32_bf16 v[80:83], v[154:157], v[210:213], v[80:83]
	v_mfma_f32_16x16x32_bf16 v[68:71], v[146:149], v[218:221], v[68:71]
	v_mfma_f32_16x16x32_bf16 v[64:67], v[154:157], v[218:221], v[64:67]
	v_mfma_f32_16x16x32_bf16 v[124:127], v[158:161], v[182:185], v[120:123]
	v_mfma_f32_16x16x32_bf16 v[100:103], v[150:153], v[190:193], v[100:103]
	v_mfma_f32_16x16x32_bf16 v[96:99], v[158:161], v[190:193], v[96:99]
	v_mfma_f32_16x16x32_bf16 v[84:87], v[150:153], v[214:217], v[84:87]
	v_mfma_f32_16x16x32_bf16 v[80:83], v[158:161], v[214:217], v[80:83]
	v_mfma_f32_16x16x32_bf16 v[68:71], v[150:153], v[222:225], v[68:71]
	v_mfma_f32_16x16x32_bf16 v[64:67], v[158:161], v[222:225], v[64:67]
	s_barrier
	s_add_i32 s60, vcc_lo, s39
	v_lshl_add_u64 v[210:211], s[84:85], 0, v[198:199]
	s_mov_b32 m0, s60
	ds_read_b128 v[186:189], v236 offset:16384
	ds_read_b128 v[190:193], v236 offset:17408
	ds_read_b128 v[178:181], v236 offset:18432
	ds_read_b128 v[182:185], v236 offset:19456
	ds_read_b128 v[138:141], v236 offset:20480
	ds_read_b128 v[142:145], v236 offset:21504
	ds_read_b128 v[120:123], v236 offset:22528
	ds_read_b128 v[134:137], v236 offset:23552
	global_load_lds_dwordx4 v[210:211], off
	s_add_i32 m0, s60, 0x2000
	s_add_u32 s60, s84, 0x80000
	v_lshl_add_u64 v[212:213], s[84:85], 0, v[200:201]
	s_addc_u32 s61, s85, 0
	s_add_i32 s81, s81, s39
	global_load_lds_dwordx4 v[212:213], off
	v_lshl_add_u64 v[214:215], s[60:61], 0, v[198:199]
	s_mov_b32 m0, s81
	v_lshl_add_u64 v[216:217], s[24:25], 0, v[200:201]
	global_load_lds_dwordx4 v[214:215], off
	v_lshl_add_u64 v[214:215], s[60:61], 0, v[200:201]
	s_add_i32 m0, s81, 0x2000
	v_cndmask_b32_e64 v128, 0, 1, s[96:97]
	global_load_lds_dwordx4 v[214:215], off
	v_lshl_add_u64 v[214:215], s[24:25], 0, v[198:199]
	s_mov_b32 m0, s53
	v_cmp_ne_u32_e64 s[60:61], 1, v128
	global_load_lds_dwordx4 v[214:215], off
	s_mov_b32 m0, s88
	s_andn2_b64 vcc, exec, s[96:97]
	global_load_lds_dwordx4 v[216:217], off
	s_waitcnt vmcnt(8) lgkmcnt(0)
	s_barrier
	s_cbranch_vccnz .LBB0_971
	s_waitcnt lgkmcnt(0)
	v_mfma_f32_16x16x32_bf16 v[60:63], v[162:165], v[186:189], v[60:63]
	v_mfma_f32_16x16x32_bf16 v[56:59], v[170:173], v[186:189], v[56:59]
	v_mfma_f32_16x16x32_bf16 v[44:47], v[162:165], v[178:181], v[44:47]
	v_mfma_f32_16x16x32_bf16 v[40:43], v[170:173], v[178:181], v[40:43]
	v_mfma_f32_16x16x32_bf16 v[28:31], v[162:165], v[138:141], v[28:31]
	v_mfma_f32_16x16x32_bf16 v[24:27], v[170:173], v[138:141], v[24:27]
	v_mfma_f32_16x16x32_bf16 v[12:15], v[162:165], v[120:123], v[12:15]
	v_mfma_f32_16x16x32_bf16 v[8:11], v[170:173], v[120:123], v[8:11]
	v_mfma_f32_16x16x32_bf16 v[60:63], v[166:169], v[190:193], v[60:63]
	v_mfma_f32_16x16x32_bf16 v[56:59], v[174:177], v[190:193], v[56:59]
	v_mfma_f32_16x16x32_bf16 v[44:47], v[166:169], v[182:185], v[44:47]
	v_mfma_f32_16x16x32_bf16 v[40:43], v[174:177], v[182:185], v[40:43]
	v_mfma_f32_16x16x32_bf16 v[28:31], v[166:169], v[142:145], v[28:31]
	v_mfma_f32_16x16x32_bf16 v[24:27], v[174:177], v[142:145], v[24:27]
	v_mfma_f32_16x16x32_bf16 v[12:15], v[166:169], v[134:137], v[12:15]
	v_mfma_f32_16x16x32_bf16 v[8:11], v[174:177], v[134:137], v[8:11]
	v_mfma_f32_16x16x32_bf16 v[52:55], v[146:149], v[186:189], v[52:55]
	v_mfma_f32_16x16x32_bf16 v[48:51], v[154:157], v[186:189], v[48:51]
	v_mfma_f32_16x16x32_bf16 v[36:39], v[146:149], v[178:181], v[36:39]
	v_mfma_f32_16x16x32_bf16 v[32:35], v[154:157], v[178:181], v[32:35]
	v_mfma_f32_16x16x32_bf16 v[20:23], v[146:149], v[138:141], v[20:23]
	v_mfma_f32_16x16x32_bf16 v[16:19], v[154:157], v[138:141], v[16:19]
	v_mfma_f32_16x16x32_bf16 v[4:7], v[146:149], v[120:123], v[4:7]
	v_mfma_f32_16x16x32_bf16 v[0:3], v[154:157], v[120:123], v[0:3]
	v_mfma_f32_16x16x32_bf16 v[52:55], v[150:153], v[190:193], v[52:55]
	v_mfma_f32_16x16x32_bf16 v[48:51], v[158:161], v[190:193], v[48:51]
	v_mfma_f32_16x16x32_bf16 v[36:39], v[150:153], v[182:185], v[36:39]
	v_mfma_f32_16x16x32_bf16 v[32:35], v[158:161], v[182:185], v[32:35]
	v_mfma_f32_16x16x32_bf16 v[20:23], v[150:153], v[142:145], v[20:23]
	v_mfma_f32_16x16x32_bf16 v[16:19], v[158:161], v[142:145], v[16:19]
	v_mfma_f32_16x16x32_bf16 v[4:7], v[150:153], v[134:137], v[4:7]
	v_mfma_f32_16x16x32_bf16 v[0:3], v[158:161], v[134:137], v[0:3]
.LBB0_971:
	s_barrier
	s_add_i32 s81, 0, 0x18000
	s_waitcnt lgkmcnt(0)
	v_add_u32_e32 v120, s81, v234
	s_add_i32 vcc_lo, 0, 0x1c000
	ds_read_b128 v[162:165], v120
	ds_read_b128 v[166:169], v120 offset:1024
	ds_read_b128 v[170:173], v120 offset:2048
	ds_read_b128 v[174:177], v120 offset:3072
	v_add_u32_e32 v120, vcc_lo, v234
	ds_read_b128 v[146:149], v120
	ds_read_b128 v[150:153], v120 offset:1024
	ds_read_b128 v[154:157], v120 offset:2048
	ds_read_b128 v[158:161], v120 offset:3072
	s_and_b64 s[26:27], s[26:27], exec
	s_cselect_b32 s27, s72, s20
	s_cselect_b32 s26, 0, s21
	s_add_u32 s24, s24, s27
	s_addc_u32 s25, s25, s26
	s_mov_b32 m0, s89
	v_lshl_add_u64 v[120:121], s[24:25], 0, v[198:199]
	ds_read_b128 v[178:181], v236 offset:32768
	ds_read_b128 v[182:185], v236 offset:33792
	ds_read_b128 v[186:189], v236 offset:34816
	ds_read_b128 v[190:193], v236 offset:35840
	ds_read_b128 v[218:221], v236 offset:36864
	ds_read_b128 v[222:225], v236 offset:37888
	ds_read_b128 v[226:229], v236 offset:38912
	ds_read_b128 v[238:241], v236 offset:39936
	global_load_lds_dwordx4 v[120:121], off
	s_mov_b32 m0, s90
	v_lshl_add_u64 v[120:121], s[24:25], 0, v[200:201]
	global_load_lds_dwordx4 v[120:121], off
	s_waitcnt vmcnt(8) lgkmcnt(0)
	s_barrier
	v_mfma_f32_16x16x32_bf16 v[104:107], v[162:165], v[178:181], v[104:107]
	v_mfma_f32_16x16x32_bf16 v[142:145], v[166:169], v[182:185], v[104:107]
	v_mfma_f32_16x16x32_bf16 v[104:107], v[170:173], v[178:181], v[108:111]
	v_mfma_f32_16x16x32_bf16 v[138:141], v[174:177], v[182:185], v[104:107]
	v_mfma_f32_16x16x32_bf16 v[104:107], v[162:165], v[186:189], v[116:119]
	v_mfma_f32_16x16x32_bf16 v[120:123], v[166:169], v[190:193], v[104:107]
	v_mfma_f32_16x16x32_bf16 v[104:107], v[170:173], v[186:189], v[112:115]
	v_mfma_f32_16x16x32_bf16 v[92:95], v[162:165], v[218:221], v[92:95]
	v_mfma_f32_16x16x32_bf16 v[88:91], v[170:173], v[218:221], v[88:91]
	v_mfma_f32_16x16x32_bf16 v[76:79], v[162:165], v[226:229], v[76:79]
	v_mfma_f32_16x16x32_bf16 v[72:75], v[170:173], v[226:229], v[72:75]
	v_mfma_f32_16x16x32_bf16 v[112:115], v[174:177], v[190:193], v[104:107]
	v_mfma_f32_16x16x32_bf16 v[92:95], v[166:169], v[222:225], v[92:95]
	v_mfma_f32_16x16x32_bf16 v[88:91], v[174:177], v[222:225], v[88:91]
	v_mfma_f32_16x16x32_bf16 v[76:79], v[166:169], v[238:241], v[76:79]
	v_mfma_f32_16x16x32_bf16 v[72:75], v[174:177], v[238:241], v[72:75]
	v_mfma_f32_16x16x32_bf16 v[104:107], v[146:149], v[178:181], v[130:133]
	v_mfma_f32_16x16x32_bf16 v[134:137], v[150:153], v[182:185], v[104:107]
	v_mfma_f32_16x16x32_bf16 v[104:107], v[154:157], v[178:181], v[124:127]
	v_mfma_f32_16x16x32_bf16 v[100:103], v[146:149], v[186:189], v[100:103]
	v_mfma_f32_16x16x32_bf16 v[96:99], v[154:157], v[186:189], v[96:99]
	v_mfma_f32_16x16x32_bf16 v[84:87], v[146:149], v[218:221], v[84:87]
	v_mfma_f32_16x16x32_bf16 v[80:83], v[154:157], v[218:221], v[80:83]
	v_mfma_f32_16x16x32_bf16 v[68:71], v[146:149], v[226:229], v[68:71]
	v_mfma_f32_16x16x32_bf16 v[64:67], v[154:157], v[226:229], v[64:67]
	v_mfma_f32_16x16x32_bf16 v[124:127], v[158:161], v[182:185], v[104:107]
	v_mfma_f32_16x16x32_bf16 v[100:103], v[150:153], v[190:193], v[100:103]
	v_mfma_f32_16x16x32_bf16 v[96:99], v[158:161], v[190:193], v[96:99]
	v_mfma_f32_16x16x32_bf16 v[84:87], v[150:153], v[222:225], v[84:87]
	v_mfma_f32_16x16x32_bf16 v[80:83], v[158:161], v[222:225], v[80:83]
	v_mfma_f32_16x16x32_bf16 v[68:71], v[150:153], v[238:241], v[68:71]
	v_mfma_f32_16x16x32_bf16 v[64:67], v[158:161], v[238:241], v[64:67]
	s_barrier
	s_add_i32 s24, s81, s39
	v_lshl_add_u64 v[210:211], v[210:211], 0, s[42:43]
	s_mov_b32 m0, s24
	ds_read_b128 v[186:189], v236 offset:49152
	ds_read_b128 v[190:193], v236 offset:50176
	ds_read_b128 v[178:181], v236 offset:51200
	ds_read_b128 v[182:185], v236 offset:52224
	ds_read_b128 v[116:119], v236 offset:53248
	ds_read_b128 v[130:133], v236 offset:54272
	ds_read_b128 v[104:107], v236 offset:55296
	ds_read_b128 v[108:111], v236 offset:56320
	global_load_lds_dwordx4 v[210:211], off
	s_add_i32 m0, s24, 0x2000
	s_add_u32 s24, s84, 0x80080
	v_lshl_add_u64 v[210:211], v[212:213], 0, s[42:43]
	s_addc_u32 s25, s85, 0
	s_add_i32 s26, vcc_lo, s39
	global_load_lds_dwordx4 v[210:211], off
	v_lshl_add_u64 v[210:211], s[24:25], 0, v[198:199]
	s_mov_b32 m0, s26
	s_and_b64 vcc, exec, s[60:61]
	global_load_lds_dwordx4 v[210:211], off
	s_add_i32 m0, s26, 0x2000
	v_lshl_add_u64 v[210:211], s[24:25], 0, v[200:201]
	global_load_lds_dwordx4 v[210:211], off
	s_mov_b32 m0, s94
	v_lshl_add_u64 v[210:211], v[214:215], 0, s[42:43]
	global_load_lds_dwordx4 v[210:211], off
	s_mov_b32 m0, s33
	v_lshl_add_u64 v[210:211], v[216:217], 0, s[42:43]
	global_load_lds_dwordx4 v[210:211], off
	s_waitcnt vmcnt(8) lgkmcnt(0)
	s_barrier
	s_cbranch_vccnz .LBB0_968
	s_waitcnt lgkmcnt(0)
	v_mfma_f32_16x16x32_bf16 v[60:63], v[162:165], v[186:189], v[60:63]
	v_mfma_f32_16x16x32_bf16 v[56:59], v[170:173], v[186:189], v[56:59]
	v_mfma_f32_16x16x32_bf16 v[44:47], v[162:165], v[178:181], v[44:47]
	v_mfma_f32_16x16x32_bf16 v[40:43], v[170:173], v[178:181], v[40:43]
	v_mfma_f32_16x16x32_bf16 v[28:31], v[162:165], v[116:119], v[28:31]
	v_mfma_f32_16x16x32_bf16 v[24:27], v[170:173], v[116:119], v[24:27]
	v_mfma_f32_16x16x32_bf16 v[12:15], v[162:165], v[104:107], v[12:15]
	v_mfma_f32_16x16x32_bf16 v[8:11], v[170:173], v[104:107], v[8:11]
	v_mfma_f32_16x16x32_bf16 v[60:63], v[166:169], v[190:193], v[60:63]
	v_mfma_f32_16x16x32_bf16 v[56:59], v[174:177], v[190:193], v[56:59]
	v_mfma_f32_16x16x32_bf16 v[44:47], v[166:169], v[182:185], v[44:47]
	v_mfma_f32_16x16x32_bf16 v[40:43], v[174:177], v[182:185], v[40:43]
	v_mfma_f32_16x16x32_bf16 v[28:31], v[166:169], v[130:133], v[28:31]
	v_mfma_f32_16x16x32_bf16 v[24:27], v[174:177], v[130:133], v[24:27]
	v_mfma_f32_16x16x32_bf16 v[12:15], v[166:169], v[108:111], v[12:15]
	v_mfma_f32_16x16x32_bf16 v[8:11], v[174:177], v[108:111], v[8:11]
	v_mfma_f32_16x16x32_bf16 v[52:55], v[146:149], v[186:189], v[52:55]
	v_mfma_f32_16x16x32_bf16 v[48:51], v[154:157], v[186:189], v[48:51]
	v_mfma_f32_16x16x32_bf16 v[36:39], v[146:149], v[178:181], v[36:39]
	v_mfma_f32_16x16x32_bf16 v[32:35], v[154:157], v[178:181], v[32:35]
	v_mfma_f32_16x16x32_bf16 v[20:23], v[146:149], v[116:119], v[20:23]
	v_mfma_f32_16x16x32_bf16 v[16:19], v[154:157], v[116:119], v[16:19]
	v_mfma_f32_16x16x32_bf16 v[4:7], v[146:149], v[104:107], v[4:7]
	v_mfma_f32_16x16x32_bf16 v[0:3], v[154:157], v[104:107], v[0:3]
	v_mfma_f32_16x16x32_bf16 v[52:55], v[150:153], v[190:193], v[52:55]
	v_mfma_f32_16x16x32_bf16 v[48:51], v[158:161], v[190:193], v[48:51]
	v_mfma_f32_16x16x32_bf16 v[36:39], v[150:153], v[182:185], v[36:39]
	v_mfma_f32_16x16x32_bf16 v[32:35], v[158:161], v[182:185], v[32:35]
	v_mfma_f32_16x16x32_bf16 v[20:23], v[150:153], v[130:133], v[20:23]
	v_mfma_f32_16x16x32_bf16 v[16:19], v[158:161], v[130:133], v[16:19]
	v_mfma_f32_16x16x32_bf16 v[4:7], v[150:153], v[108:111], v[4:7]
	v_mfma_f32_16x16x32_bf16 v[0:3], v[158:161], v[108:111], v[0:3]
	s_branch .LBB0_968

.LBB0_1443:
	s_lshl_b32 s72, s19, 7
	s_add_u32 s29, s76, s72
	s_addc_u32 s30, s77, 0
	s_add_u32 s22, s29, 0x100
	s_addc_u32 s23, s30, 0
	v_lshl_add_u64 v[144:145], v[142:143], 0, s[72:73]
	s_and_b64 s[2:3], s[60:61], exec
	v_lshl_add_u64 v[144:145], v[144:145], 0, s[46:47]
	s_cselect_b32 s23, s67, s23
	s_cselect_b32 s22, s66, s22
	v_cndmask_b32_e64 v145, v145, v141, s[60:61]
	v_cndmask_b32_e64 v144, v144, v140, s[60:61]
	s_add_i32 s60, 0, 0x10000
	v_add_u32_e32 v128, s60, v147
	s_add_i32 s61, 0, 0x14000
	ds_read_b128 v[150:153], v128
	ds_read_b128 v[154:157], v128 offset:1024
	ds_read_b128 v[158:161], v128 offset:2048
	ds_read_b128 v[162:165], v128 offset:3072
	v_add_u32_e32 v128, s61, v147
	ds_read_b128 v[166:169], v128
	ds_read_b128 v[170:173], v128 offset:1024
	ds_read_b128 v[174:177], v128 offset:2048
	ds_read_b128 v[178:181], v128 offset:3072
	s_add_u32 s2, s29, 0x20080
	s_addc_u32 s3, s30, 0
	v_lshl_add_u64 v[194:195], s[2:3], 0, v[130:131]
	s_add_i32 m0, s35, 0xc000
	ds_read_b128 v[182:185], v148
	ds_read_b128 v[186:189], v148 offset:1024
	ds_read_b128 v[190:193], v148 offset:2048
	ds_read_b128 v[198:201], v148 offset:3072
	ds_read_b128 v[202:205], v148 offset:4096
	ds_read_b128 v[206:209], v148 offset:5120
	ds_read_b128 v[210:213], v148 offset:6144
	ds_read_b128 v[214:217], v148 offset:7168
	global_load_lds_dwordx4 v[194:195], off
	s_add_i32 m0, s35, 0xe000
	v_lshl_add_u64 v[194:195], s[2:3], 0, v[134:135]
	global_load_lds_dwordx4 v[194:195], off
	s_waitcnt vmcnt(8) lgkmcnt(0)
	s_barrier
	v_mfma_f32_16x16x32_bf16 v[124:127], v[150:153], v[182:185], v[124:127]
	v_mfma_f32_16x16x32_bf16 v[120:123], v[158:161], v[182:185], v[120:123]
	v_mfma_f32_16x16x32_bf16 v[112:115], v[150:153], v[190:193], v[112:115]
	v_mfma_f32_16x16x32_bf16 v[104:107], v[158:161], v[190:193], v[104:107]
	v_mfma_f32_16x16x32_bf16 v[96:99], v[150:153], v[202:205], v[96:99]
	v_mfma_f32_16x16x32_bf16 v[88:91], v[158:161], v[202:205], v[88:91]
	v_mfma_f32_16x16x32_bf16 v[80:83], v[150:153], v[210:213], v[80:83]
	v_mfma_f32_16x16x32_bf16 v[72:75], v[158:161], v[210:213], v[72:75]
	v_mfma_f32_16x16x32_bf16 v[124:127], v[154:157], v[186:189], v[124:127]
	v_mfma_f32_16x16x32_bf16 v[120:123], v[162:165], v[186:189], v[120:123]
	v_mfma_f32_16x16x32_bf16 v[112:115], v[154:157], v[198:201], v[112:115]
	v_mfma_f32_16x16x32_bf16 v[104:107], v[162:165], v[198:201], v[104:107]
	v_mfma_f32_16x16x32_bf16 v[96:99], v[154:157], v[206:209], v[96:99]
	v_mfma_f32_16x16x32_bf16 v[88:91], v[162:165], v[206:209], v[88:91]
	v_mfma_f32_16x16x32_bf16 v[80:83], v[154:157], v[214:217], v[80:83]
	v_mfma_f32_16x16x32_bf16 v[72:75], v[162:165], v[214:217], v[72:75]
	v_mfma_f32_16x16x32_bf16 v[116:119], v[166:169], v[182:185], v[116:119]
	v_mfma_f32_16x16x32_bf16 v[108:111], v[174:177], v[182:185], v[108:111]
	v_mfma_f32_16x16x32_bf16 v[100:103], v[166:169], v[190:193], v[100:103]
	v_mfma_f32_16x16x32_bf16 v[92:95], v[174:177], v[190:193], v[92:95]
	v_mfma_f32_16x16x32_bf16 v[84:87], v[166:169], v[202:205], v[84:87]
	v_mfma_f32_16x16x32_bf16 v[76:79], v[174:177], v[202:205], v[76:79]
	v_mfma_f32_16x16x32_bf16 v[68:71], v[166:169], v[210:213], v[68:71]
	v_mfma_f32_16x16x32_bf16 v[64:67], v[174:177], v[210:213], v[64:67]
	v_mfma_f32_16x16x32_bf16 v[116:119], v[170:173], v[186:189], v[116:119]
	v_mfma_f32_16x16x32_bf16 v[108:111], v[178:181], v[186:189], v[108:111]
	v_mfma_f32_16x16x32_bf16 v[100:103], v[170:173], v[198:201], v[100:103]
	v_mfma_f32_16x16x32_bf16 v[92:95], v[178:181], v[198:201], v[92:95]
	v_mfma_f32_16x16x32_bf16 v[84:87], v[170:173], v[206:209], v[84:87]
	v_mfma_f32_16x16x32_bf16 v[76:79], v[178:181], v[206:209], v[76:79]
	v_mfma_f32_16x16x32_bf16 v[68:71], v[170:173], v[214:217], v[68:71]
	v_mfma_f32_16x16x32_bf16 v[64:67], v[178:181], v[214:217], v[64:67]
	s_barrier
	s_add_i32 s2, s60, s33
	v_lshl_add_u64 v[194:195], v[144:145], 0, v[132:133]
	s_mov_b32 m0, s2
	ds_read_b128 v[182:185], v148 offset:16384
	ds_read_b128 v[186:189], v148 offset:17408
	ds_read_b128 v[190:193], v148 offset:18432
	ds_read_b128 v[198:201], v148 offset:19456
	ds_read_b128 v[202:205], v148 offset:20480
	ds_read_b128 v[206:209], v148 offset:21504
	ds_read_b128 v[210:213], v148 offset:22528
	ds_read_b128 v[214:217], v148 offset:23552
	global_load_lds_dwordx4 v[194:195], off
	v_lshl_add_u64 v[196:197], v[144:145], 0, v[136:137]
	s_add_i32 m0, s2, 0x2000
	v_lshl_add_u64 v[218:219], v[144:145], 0, s[48:49]
	s_add_i32 s2, s61, s33
	global_load_lds_dwordx4 v[196:197], off
	v_lshl_add_u64 v[220:221], v[218:219], 0, v[132:133]
	s_mov_b32 m0, s2
	v_lshl_add_u64 v[218:219], v[218:219], 0, v[136:137]
	global_load_lds_dwordx4 v[220:221], off
	s_add_i32 m0, s2, 0x2000
	v_lshl_add_u64 v[220:221], s[22:23], 0, v[134:135]
	global_load_lds_dwordx4 v[218:219], off
	s_mov_b32 m0, s35
	v_lshl_add_u64 v[218:219], s[22:23], 0, v[130:131]
	global_load_lds_dwordx4 v[218:219], off
	s_mov_b32 m0, s36
	s_nop 0
	global_load_lds_dwordx4 v[220:221], off
	s_waitcnt vmcnt(8) lgkmcnt(0)
	s_barrier
	v_mfma_f32_16x16x32_bf16 v[60:63], v[150:153], v[182:185], v[60:63]
	v_mfma_f32_16x16x32_bf16 v[56:59], v[158:161], v[182:185], v[56:59]
	v_mfma_f32_16x16x32_bf16 v[48:51], v[150:153], v[190:193], v[48:51]
	v_mfma_f32_16x16x32_bf16 v[40:43], v[158:161], v[190:193], v[40:43]
	v_mfma_f32_16x16x32_bf16 v[32:35], v[150:153], v[202:205], v[32:35]
	v_mfma_f32_16x16x32_bf16 v[24:27], v[158:161], v[202:205], v[24:27]
	v_mfma_f32_16x16x32_bf16 v[16:19], v[150:153], v[210:213], v[16:19]
	v_mfma_f32_16x16x32_bf16 v[8:11], v[158:161], v[210:213], v[8:11]
	v_mfma_f32_16x16x32_bf16 v[60:63], v[154:157], v[186:189], v[60:63]
	v_mfma_f32_16x16x32_bf16 v[56:59], v[162:165], v[186:189], v[56:59]
	v_mfma_f32_16x16x32_bf16 v[48:51], v[154:157], v[198:201], v[48:51]
	v_mfma_f32_16x16x32_bf16 v[40:43], v[162:165], v[198:201], v[40:43]
	v_mfma_f32_16x16x32_bf16 v[32:35], v[154:157], v[206:209], v[32:35]
	v_mfma_f32_16x16x32_bf16 v[24:27], v[162:165], v[206:209], v[24:27]
	v_mfma_f32_16x16x32_bf16 v[16:19], v[154:157], v[214:217], v[16:19]
	v_mfma_f32_16x16x32_bf16 v[8:11], v[162:165], v[214:217], v[8:11]
	v_mfma_f32_16x16x32_bf16 v[52:55], v[166:169], v[182:185], v[52:55]
	v_mfma_f32_16x16x32_bf16 v[44:47], v[174:177], v[182:185], v[44:47]
	v_mfma_f32_16x16x32_bf16 v[36:39], v[166:169], v[190:193], v[36:39]
	v_mfma_f32_16x16x32_bf16 v[28:31], v[174:177], v[190:193], v[28:31]
	v_mfma_f32_16x16x32_bf16 v[20:23], v[166:169], v[202:205], v[20:23]
	v_mfma_f32_16x16x32_bf16 v[12:15], v[174:177], v[202:205], v[12:15]
	v_mfma_f32_16x16x32_bf16 v[4:7], v[166:169], v[210:213], v[4:7]
	v_mfma_f32_16x16x32_bf16 v[0:3], v[174:177], v[210:213], v[0:3]
	v_mfma_f32_16x16x32_bf16 v[52:55], v[170:173], v[186:189], v[52:55]
	v_mfma_f32_16x16x32_bf16 v[44:47], v[178:181], v[186:189], v[44:47]
	v_mfma_f32_16x16x32_bf16 v[36:39], v[170:173], v[198:201], v[36:39]
	v_mfma_f32_16x16x32_bf16 v[28:31], v[178:181], v[198:201], v[28:31]
	v_mfma_f32_16x16x32_bf16 v[20:23], v[170:173], v[206:209], v[20:23]
	v_mfma_f32_16x16x32_bf16 v[12:15], v[178:181], v[206:209], v[12:15]
	v_mfma_f32_16x16x32_bf16 v[4:7], v[170:173], v[214:217], v[4:7]
	v_mfma_f32_16x16x32_bf16 v[0:3], v[178:181], v[214:217], v[0:3]
	s_barrier
	s_add_i32 s29, 0, 0x18000
	v_add_u32_e32 v128, s29, v147
	s_add_i32 s30, 0, 0x1c000
	ds_read_b128 v[150:153], v128
	ds_read_b128 v[154:157], v128 offset:1024
	ds_read_b128 v[158:161], v128 offset:2048
	ds_read_b128 v[162:165], v128 offset:3072
	v_add_u32_e32 v128, s30, v147
	ds_read_b128 v[166:169], v128
	ds_read_b128 v[170:173], v128 offset:1024
	ds_read_b128 v[174:177], v128 offset:2048
	ds_read_b128 v[178:181], v128 offset:3072
	s_add_u32 s2, s22, 0x20000
	s_addc_u32 s3, s23, 0
	s_mov_b32 m0, s37
	v_lshl_add_u64 v[222:223], s[2:3], 0, v[130:131]
	ds_read_b128 v[182:185], v148 offset:32768
	ds_read_b128 v[186:189], v148 offset:33792
	ds_read_b128 v[190:193], v148 offset:34816
	ds_read_b128 v[198:201], v148 offset:35840
	ds_read_b128 v[202:205], v148 offset:36864
	ds_read_b128 v[206:209], v148 offset:37888
	ds_read_b128 v[210:213], v148 offset:38912
	ds_read_b128 v[214:217], v148 offset:39936
	global_load_lds_dwordx4 v[222:223], off
	s_mov_b32 m0, s38
	v_lshl_add_u64 v[222:223], s[2:3], 0, v[134:135]
	global_load_lds_dwordx4 v[222:223], off
	s_waitcnt vmcnt(8) lgkmcnt(0)
	s_barrier
	v_mfma_f32_16x16x32_bf16 v[124:127], v[150:153], v[182:185], v[124:127]
	v_mfma_f32_16x16x32_bf16 v[120:123], v[158:161], v[182:185], v[120:123]
	v_mfma_f32_16x16x32_bf16 v[112:115], v[150:153], v[190:193], v[112:115]
	v_mfma_f32_16x16x32_bf16 v[104:107], v[158:161], v[190:193], v[104:107]
	v_mfma_f32_16x16x32_bf16 v[96:99], v[150:153], v[202:205], v[96:99]
	v_mfma_f32_16x16x32_bf16 v[88:91], v[158:161], v[202:205], v[88:91]
	v_mfma_f32_16x16x32_bf16 v[80:83], v[150:153], v[210:213], v[80:83]
	v_mfma_f32_16x16x32_bf16 v[72:75], v[158:161], v[210:213], v[72:75]
	v_mfma_f32_16x16x32_bf16 v[124:127], v[154:157], v[186:189], v[124:127]
	v_mfma_f32_16x16x32_bf16 v[120:123], v[162:165], v[186:189], v[120:123]
	v_mfma_f32_16x16x32_bf16 v[112:115], v[154:157], v[198:201], v[112:115]
	v_mfma_f32_16x16x32_bf16 v[104:107], v[162:165], v[198:201], v[104:107]
	v_mfma_f32_16x16x32_bf16 v[96:99], v[154:157], v[206:209], v[96:99]
	v_mfma_f32_16x16x32_bf16 v[88:91], v[162:165], v[206:209], v[88:91]
	v_mfma_f32_16x16x32_bf16 v[80:83], v[154:157], v[214:217], v[80:83]
	v_mfma_f32_16x16x32_bf16 v[72:75], v[162:165], v[214:217], v[72:75]
	v_mfma_f32_16x16x32_bf16 v[116:119], v[166:169], v[182:185], v[116:119]
	v_mfma_f32_16x16x32_bf16 v[108:111], v[174:177], v[182:185], v[108:111]
	v_mfma_f32_16x16x32_bf16 v[100:103], v[166:169], v[190:193], v[100:103]
	v_mfma_f32_16x16x32_bf16 v[92:95], v[174:177], v[190:193], v[92:95]
	v_mfma_f32_16x16x32_bf16 v[84:87], v[166:169], v[202:205], v[84:87]
	v_mfma_f32_16x16x32_bf16 v[76:79], v[174:177], v[202:205], v[76:79]
	v_mfma_f32_16x16x32_bf16 v[68:71], v[166:169], v[210:213], v[68:71]
	v_mfma_f32_16x16x32_bf16 v[64:67], v[174:177], v[210:213], v[64:67]
	v_mfma_f32_16x16x32_bf16 v[116:119], v[170:173], v[186:189], v[116:119]
	v_mfma_f32_16x16x32_bf16 v[108:111], v[178:181], v[186:189], v[108:111]
	v_mfma_f32_16x16x32_bf16 v[100:103], v[170:173], v[198:201], v[100:103]
	v_mfma_f32_16x16x32_bf16 v[92:95], v[178:181], v[198:201], v[92:95]
	v_mfma_f32_16x16x32_bf16 v[84:87], v[170:173], v[206:209], v[84:87]
	v_mfma_f32_16x16x32_bf16 v[76:79], v[178:181], v[206:209], v[76:79]
	v_mfma_f32_16x16x32_bf16 v[68:71], v[170:173], v[214:217], v[68:71]
	v_mfma_f32_16x16x32_bf16 v[64:67], v[178:181], v[214:217], v[64:67]
	s_barrier
	s_add_i32 s2, s29, s33
	v_lshl_add_u64 v[194:195], v[194:195], 0, s[42:43]
	s_mov_b32 m0, s2
	ds_read_b128 v[182:185], v148 offset:49152
	ds_read_b128 v[186:189], v148 offset:50176
	ds_read_b128 v[190:193], v148 offset:51200
	ds_read_b128 v[198:201], v148 offset:52224
	ds_read_b128 v[202:205], v148 offset:53248
	ds_read_b128 v[206:209], v148 offset:54272
	ds_read_b128 v[210:213], v148 offset:55296
	ds_read_b128 v[214:217], v148 offset:56320
	global_load_lds_dwordx4 v[194:195], off
	v_lshl_add_u64 v[194:195], v[196:197], 0, s[42:43]
	s_add_i32 m0, s2, 0x2000
	v_lshl_add_u64 v[144:145], v[144:145], 0, s[50:51]
	s_add_i32 s2, s30, s33
	global_load_lds_dwordx4 v[194:195], off
	v_lshl_add_u64 v[194:195], v[144:145], 0, v[132:133]
	s_mov_b32 m0, s2
	v_lshl_add_u64 v[144:145], v[144:145], 0, v[136:137]
	global_load_lds_dwordx4 v[194:195], off
	s_add_i32 m0, s2, 0x2000
	s_nop 0
	global_load_lds_dwordx4 v[144:145], off
	s_mov_b32 m0, s39
	v_lshl_add_u64 v[144:145], v[218:219], 0, s[42:43]
	global_load_lds_dwordx4 v[144:145], off
	s_mov_b32 m0, s53
	v_lshl_add_u64 v[144:145], v[220:221], 0, s[42:43]
	global_load_lds_dwordx4 v[144:145], off
	s_waitcnt vmcnt(8) lgkmcnt(0)
	s_barrier
	v_mfma_f32_16x16x32_bf16 v[60:63], v[150:153], v[182:185], v[60:63]
	v_mfma_f32_16x16x32_bf16 v[56:59], v[158:161], v[182:185], v[56:59]
	v_mfma_f32_16x16x32_bf16 v[48:51], v[150:153], v[190:193], v[48:51]
	v_mfma_f32_16x16x32_bf16 v[40:43], v[158:161], v[190:193], v[40:43]
	v_mfma_f32_16x16x32_bf16 v[32:35], v[150:153], v[202:205], v[32:35]
	v_mfma_f32_16x16x32_bf16 v[24:27], v[158:161], v[202:205], v[24:27]
	v_mfma_f32_16x16x32_bf16 v[16:19], v[150:153], v[210:213], v[16:19]
	v_mfma_f32_16x16x32_bf16 v[8:11], v[158:161], v[210:213], v[8:11]
	v_mfma_f32_16x16x32_bf16 v[60:63], v[154:157], v[186:189], v[60:63]
	v_mfma_f32_16x16x32_bf16 v[56:59], v[162:165], v[186:189], v[56:59]
	v_mfma_f32_16x16x32_bf16 v[48:51], v[154:157], v[198:201], v[48:51]
	v_mfma_f32_16x16x32_bf16 v[40:43], v[162:165], v[198:201], v[40:43]
	v_mfma_f32_16x16x32_bf16 v[32:35], v[154:157], v[206:209], v[32:35]
	v_mfma_f32_16x16x32_bf16 v[24:27], v[162:165], v[206:209], v[24:27]
	v_mfma_f32_16x16x32_bf16 v[16:19], v[154:157], v[214:217], v[16:19]
	v_mfma_f32_16x16x32_bf16 v[8:11], v[162:165], v[214:217], v[8:11]
	v_mfma_f32_16x16x32_bf16 v[52:55], v[166:169], v[182:185], v[52:55]
	v_mfma_f32_16x16x32_bf16 v[44:47], v[174:177], v[182:185], v[44:47]
	v_mfma_f32_16x16x32_bf16 v[36:39], v[166:169], v[190:193], v[36:39]
	v_mfma_f32_16x16x32_bf16 v[28:31], v[174:177], v[190:193], v[28:31]
	v_mfma_f32_16x16x32_bf16 v[20:23], v[166:169], v[202:205], v[20:23]
	v_mfma_f32_16x16x32_bf16 v[12:15], v[174:177], v[202:205], v[12:15]
	v_mfma_f32_16x16x32_bf16 v[4:7], v[166:169], v[210:213], v[4:7]
	v_mfma_f32_16x16x32_bf16 v[0:3], v[174:177], v[210:213], v[0:3]
	v_mfma_f32_16x16x32_bf16 v[52:55], v[170:173], v[186:189], v[52:55]
	v_mfma_f32_16x16x32_bf16 v[44:47], v[178:181], v[186:189], v[44:47]
	v_mfma_f32_16x16x32_bf16 v[36:39], v[170:173], v[198:201], v[36:39]
	v_mfma_f32_16x16x32_bf16 v[28:31], v[178:181], v[198:201], v[28:31]
	v_mfma_f32_16x16x32_bf16 v[20:23], v[170:173], v[206:209], v[20:23]
	v_mfma_f32_16x16x32_bf16 v[12:15], v[178:181], v[206:209], v[12:15]
	v_mfma_f32_16x16x32_bf16 v[4:7], v[170:173], v[214:217], v[4:7]
	v_mfma_f32_16x16x32_bf16 v[0:3], v[178:181], v[214:217], v[0:3]
	s_barrier
	s_add_i32 s2, s19, 2
	s_cmp_gt_u32 s19, 5
	s_mov_b32 s19, s2
	s_cbranch_scc1 .LBB0_1450
